# transpose-item mapping reversed: the waves that take three items are on the lightest workers
# baseline (speedup 1.0000x reference)
; __device__ __forceinline__ void late_weight_prep(const Params& P, LAS unsigned char* lds, int lane, int wave, int gw, int NGW) {
;     ...
;         for (int it = gw; it < I_OUT + I_Q + I_O; it += NGW) {
;             int r = it;
;             if (r < I_OUT) { p0_transpose_item(P.w_out, 1024, 1024, 0, 32, (bf16*)(ws + WS_WOUT), 0, nullptr, scr, r, lane); continue; } r -= I_OUT;
;             if (r < I_Q) { p0_transpose_item(P.xattn_wq, 1024, 1024, 0, 32, (bf16*)(ws + WS_WQ), 0, P.norm_xattn_w, scr, r, lane); continue; } r -= I_Q;
;             p0_transpose_item(P.xattn_wo, 1024, 1024, 0, 32, (bf16*)(ws + WS_WO), 0, nullptr, scr, r, lane);
;         }
; __global__ void __launch_bounds__(NWAVES * 64, 2) hybrid_fwd(Params P) {
;     ...
;                 late_weight_prep(P, lds, lane, wave, w2 * NWAVES + wave, N2 * NWAVES);
.LBB0_1975:
	s_ashr_i32 s15, s14, 31
	s_cmpk_lt_i32 s16, 0x400
	s_cbranch_scc1 .LBB0_2008
	v_and_b32_e32 v1, 31, v0
	v_lshlrev_b32_e32 v20, 2, v1
	v_lshlrev_b32_e32 v1, 3, v0
	v_and_b32_e32 v1, 56, v1
	v_readlane_b32 s0, v254, 56
	v_lshlrev_b32_e32 v6, 1, v1
	v_mov_b32_e32 v7, 0
	s_mov_b32 s22, s0
	s_lshl_b32 s0, s0, 14
	v_lshrrev_b32_e32 v23, 3, v182
	v_lshl_add_u64 v[12:13], s[24:25], 0, v[6:7]
	s_mov_b64 s[6:7], 0x1200000
	v_readlane_b32 s44, v254, 40
	s_add_i32 s13, s0, 0
	v_lshrrev_b32_e32 v2, 5, v182
	v_mul_u32_u24_e32 v3, 0x84, v1
	v_lshl_add_u64 v[8:9], v[12:13], 0, s[6:7]
	v_lshlrev_b32_e32 v1, 2, v23
	s_mov_b64 s[6:7], 0xc00000
	v_readlane_b32 s45, v254, 41
	v_add3_u32 v44, s13, v3, v1
	v_lshl_add_u64 v[10:11], v[12:13], 0, s[6:7]
	s_mov_b64 s[6:7], 0xa00000
	s_cmp_lg_u64 s[44:45], 0
	v_mul_u32_u24_e32 v3, 0x84, v2
	v_lshl_add_u64 v[12:13], v[12:13], 0, s[6:7]
	v_mov_b32_e32 v21, v7
	v_readlane_b32 s52, v254, 48
	v_readlane_b32 s53, v254, 49
	v_readlane_b32 s54, v254, 50
	v_readlane_b32 s55, v254, 51
	v_readlane_b32 s56, v254, 52
	v_readlane_b32 s57, v254, 53
	v_readlane_b32 s58, v254, 54
	v_readlane_b32 s59, v254, 55
	s_cselect_b64 s[42:43], -1, 0
	v_or_b32_e32 v3, s0, v3
	s_lshl_b32 s0, s14, 8
	s_lshl_b32 s6, s22, 5
	v_add_u32_e32 v4, s13, v20
	v_lshl_add_u64 v[14:15], s[52:53], 0, v[20:21]
	v_readlane_b32 s52, v254, 24
	s_add_i32 s13, s0, s6
	s_add_i32 s13, s13, 0xffff8000
	s_lshl_b32 s0, s14, 4
	s_lshl_b32 s6, s22, 1
	v_readlane_b32 s1, v254, 57
	v_readlane_b32 s48, v254, 44
	v_readlane_b32 s49, v254, 45
	v_readlane_b32 s66, v254, 38
	v_readlane_b32 s67, v254, 39
	s_lshl_b32 s17, s26, 8
	s_add_i32 s0, s0, s6
	s_lshl_b32 s30, s26, 4
	s_mov_b32 s1, 0
	s_movk_i32 s3, 0x84
	v_or_b32_e32 v45, 8, v23
	v_or_b32_e32 v46, 16, v23
	v_or_b32_e32 v47, 24, v23
	v_lshl_add_u64 v[16:17], s[66:67], 0, v[20:21]
	v_mov_b32_e32 v1, v2
	v_add3_u32 v48, v3, v20, 0
	v_lshl_add_u64 v[20:21], s[48:49], 0, v[20:21]
	s_addk_i32 s17, 0xde00
	v_or_b32_e32 v49, 14, v2
	s_add_i32 s19, s0, 0x1f400
	s_addk_i32 s30, 0xfde0
	v_lshlrev_b32_e32 v22, 2, v2
	v_mov_b32_e32 v3, v7
	v_or_b32_e32 v50, 12, v2
	v_or_b32_e32 v51, 10, v2
	v_or_b32_e32 v52, 8, v2
	v_or_b32_e32 v53, 6, v2
	v_or_b32_e32 v54, 4, v2
	v_or_b32_e32 v55, 2, v2
	s_movk_i32 s31, 0x7fff
	s_mov_b32 s34, 0xffff0000
	s_sub_i32 s35, 0x6ef, s16
	s_lshl_b32 s13, s35, 5
	s_lshl_b32 s19, s35, 1
	s_add_i32 s19, s19, 0x1fc00
	v_readlane_b32 s46, v254, 42
	v_readlane_b32 s47, v254, 43
	v_readlane_b32 s50, v254, 46
	v_readlane_b32 s51, v254, 47
	v_readlane_b32 s53, v254, 25
	v_readlane_b32 s54, v254, 26
	v_readlane_b32 s55, v254, 27
	v_readlane_b32 s56, v254, 28
	v_readlane_b32 s57, v254, 29
	v_readlane_b32 s58, v254, 30
	v_readlane_b32 s59, v254, 31
	v_readlane_b32 s60, v254, 32
	v_readlane_b32 s61, v254, 33
	v_readlane_b32 s62, v254, 34
	v_readlane_b32 s63, v254, 35
	v_readlane_b32 s64, v254, 36
	v_readlane_b32 s65, v254, 37
	s_branch .LBB0_1978
